# generic piggyback template: 1 piece (8 dword loads + 1 store) per K-iteration in MoE gate/up GEMM loops of both layers; FFT phase converts 64 of 96 steps
# speedup vs baseline: 1.0263x; 1.0089x over previous
; __device__ __forceinline__ int tid_fresh() { int t = threadIdx.x; asm volatile("" : "+v"(t)); return t; }
;     __device__ __forceinline__ void a_off4(const Unit& u, int r0, int r1, unsigned& o00, unsigned& o01, unsigned& o10, unsigned& o11) const { o00 = a_off(u, r0); o01 = a_off(u, r1); o10 = a_off(u, HALF + r0); o11 = a_off(u, HALF + r1); }
;     __device__ __forceinline__ unsigned b_off(int R, int C) const { return (unsigned)(R * K + C) * 2u; }
;     __device__ __forceinline__ size_t b_kstep() const { return (size_t)(BK * 2); }
;     __device__ __forceinline__ size_t b_hstep() const { return (size_t)HALF * 16; }
; template <class Epi, class Sched>
; __device__ __forceinline__ void gemm_phase(LAS unsigned char* lds, const int K, const Sched& S, const Epi& E) {
;     const int tid = tid_fresh(), wid = __builtin_amdgcn_readfirstlane(tid >> 6), lane = tid & 63, wr = wid >> 2, wc = wid & 3, fr = lane & 15, fq = lane >> 4;
;     const int nt = K / BK;
;     int R0, C0, R1, C1; stage_rc(tid * 16, R0, C0); stage_rc(tid * 16 + 8192, R1, C1);
;     const int Rb0 = Epi::PERM ? ((R0 & ~31) + perm32(R0 & 31)) : R0, Rb1 = Epi::PERM ? ((R1 & ~31) + perm32(R1 & 31)) : R1;
;     const unsigned voffB0 = S.b_off(Rb0, C0), voffB1 = S.b_off(Rb1, C1);
;     const size_t kstep = (size_t)(BK * 2);
;     const size_t kstepB = S.b_kstep(), hstep = S.b_hstep();
;     const unsigned ldsw = (unsigned)wid * 1024u;
;     const int aoff = lds_byte(wr * 64 + fr, fq * 8), boff = lds_byte(wc * 32 + fr, fq * 8);
;     __device__ __forceinline__ void a_off4(const Unit& u, int r0, int r1, unsigned& o00, unsigned& o01, unsigned& o10, unsigned& o11) const {
;         const int p0 = u.pm * BM + r0, p1 = u.pm * BM + r1, p2 = p0 + HALF, p3 = p1 + HALF;
;         if (u.e >= NE) { o00 = (unsigned)p0 * (unsigned)(D * 2); o01 = (unsigned)p1 * (unsigned)(D * 2); o10 = (unsigned)p2 * (unsigned)(D * 2); o11 = (unsigned)p3 * (unsigned)(D * 2); return; }
;         const int* lp = list + u.e * T;
;         int v0 = lp[p0], v1 = lp[p1], v2 = lp[p2], v3 = lp[p3];
;         asm volatile("" : "+v"(v0), "+v"(v1), "+v"(v2), "+v"(v3));
;         const int c = cnt[u.e];
;         o00 = p0 < c ? (unsigned)v0 * (unsigned)(D * 2) : 0u; o01 = p1 < c ? (unsigned)v1 * (unsigned)(D * 2) : 0u;
;         o10 = p2 < c ? (unsigned)v2 * (unsigned)(D * 2) : 0u; o11 = p3 < c ? (unsigned)v3 * (unsigned)(D * 2) : 0u;
;     }
.LBB0_1077:
	s_or_b64 exec, exec, s[0:1]
	v_readlane_b32 s2, v254, 5
	v_readlane_b32 s0, v254, 0
	s_and_b32 s3, s2, 3
	v_readlane_b32 s1, v254, 1
	s_lshl_b32 s29, s28, 2
	v_writelane_b32 v254, s3, 27
	s_lshl_b32 s3, s3, 12
	v_mov_b32_e32 v6, v0
	s_waitcnt lgkmcnt(0)
	s_barrier
	v_readlane_b32 s84, v254, 0
	v_readlane_b32 s85, v254, 1
	s_nop 1
	s_load_dwordx2 s[74:75], s[84:85], 0xd8
	s_load_dwordx2 s[76:77], s[84:85], 0xe0
	s_load_dwordx2 s[78:79], s[84:85], 0x118
	v_and_b32_e32 v252, 63, v0
	v_lshrrev_b32_e32 v253, 6, v0
	v_lshlrev_b32_e32 v238, 2, v252
	v_lshlrev_b32_e32 v252, 4, v252
	v_add_u32_e32 v239, 0x800, v238
	v_add_u32_e32 v240, 0x1000, v238
	v_add_u32_e32 v241, 0x1800, v238
	v_readlane_b32 s86, v254, 4
	v_readlane_b32 s87, v255, 40
	v_readfirstlane_b32 s88, v253
	s_nop 3
	s_lshl_b32 s71, s86, 3
	s_lshl_b32 s87, s87, 3
	s_add_u32 s87, s87, s88
	s_add_u32 s70, s87, 0x20000
	s_mov_b32 s80, 0
	s_mov_b32 s82, 0
	s_mov_b32 s90, 0
	s_waitcnt lgkmcnt(0)
	v_writelane_b32 v255, s3, 24
	s_cmp_lt_i32 s2, s29
	s_nop 0
	v_readfirstlane_b32 s30, v6
	s_cbranch_scc0 .LBB0_1099
	v_ashrrev_i32_e32 v1, 31, v6
	v_lshrrev_b32_e32 v1, 26, v1
	v_add_u32_e32 v1, v6, v1
	v_ashrrev_i32_e32 v9, 6, v1
	v_bfe_i32 v1, v6, 27, 1
	v_lshlrev_b32_e32 v2, 4, v6
	v_lshrrev_b32_e32 v1, 22, v1
	v_add_u32_e32 v1, v2, v1
	v_and_b32_e32 v1, 0xfffffc00, v1
	v_sub_u32_e32 v1, v2, v1
	v_lshrrev_b32_e32 v3, 4, v1
	v_bitop3_b32 v10, v3, v1, 32 bitop3:0x6c
	v_ashrrev_i32_e32 v1, 31, v1
	v_lshrrev_b32_e32 v1, 26, v1
	s_load_dwordx2 s[0:1], s[0:1], 0x118
	v_lshlrev_b32_e32 v3, 3, v9
	v_add_u32_e32 v1, v10, v1
	v_and_b32_e32 v3, -16, v3
	v_ashrrev_i32_e32 v8, 6, v1
	v_add_u32_e32 v2, 0x2000, v2
	v_add_u32_e32 v1, v8, v3
	v_ashrrev_i32_e32 v3, 31, v2
	v_lshrrev_b32_e32 v3, 22, v3
	v_add_u32_e32 v3, v2, v3
	s_waitcnt lgkmcnt(0)
	s_add_u32 s31, s0, 0x3ec30000
	v_ashrrev_i32_e32 v11, 10, v3
	v_readlane_b32 s3, v254, 5
	s_addc_u32 s33, s1, 0
	v_mul_i32_i24_e32 v3, 0x400, v11
	s_and_b32 s2, s3, -4
	v_sub_u32_e32 v2, v2, v3
	s_add_i32 s2, s2, 0
	v_lshrrev_b32_e32 v3, 4, v2
	s_add_i32 s2, s2, 0x21160
	v_bitop3_b32 v12, v3, v2, 32 bitop3:0x6c
	v_mov_b32_e32 v3, s2
	ds_read_b32 v3, v3
	v_ashrrev_i32_e32 v4, 31, v12
	v_lshrrev_b32_e32 v4, 26, v4
	v_lshlrev_b32_e32 v2, 3, v11
	v_add_u32_e32 v4, v12, v4
	s_waitcnt lgkmcnt(0)
	v_lshlrev_b32_e32 v5, 2, v3
	v_add_u32_e32 v5, 0, v5
	v_add_u32_e32 v5, 0x21040, v5
	ds_read_b32 v5, v5
	v_and_b32_e32 v2, -16, v2
	v_ashrrev_i32_e32 v13, 6, v4
	s_ashr_i32 s8, s3, 2
	v_add_u32_e32 v146, v13, v2
	s_waitcnt lgkmcnt(0)
	v_sub_u32_e32 v2, s8, v5
	v_lshlrev_b32_e32 v7, 8, v2
	v_add_u32_e32 v2, v7, v1
	v_add_u32_e32 v4, v7, v146
	v_cmp_gt_i32_e32 vcc, 64, v3
	v_readfirstlane_b32 s6, v3
	v_add_u32_e32 v14, 0x80, v2
	v_add_u32_e32 v15, 0x80, v4
	s_cbranch_vccz .LBB0_1080
	s_lshl_b32 s2, s6, 13
	s_ashr_i32 s3, s2, 31
	s_lshl_b64 s[2:3], s[2:3], 2
	s_add_u32 s2, s31, s2
	s_addc_u32 s3, s33, s3
	v_ashrrev_i32_e32 v3, 31, v2
	v_lshl_add_u64 v[16:17], v[2:3], 2, s[2:3]
	v_ashrrev_i32_e32 v5, 31, v4
	v_lshl_add_u64 v[18:19], v[4:5], 2, s[2:3]
	global_load_dword v3, v[16:17], off
	global_load_dword v5, v[18:19], off
	global_load_dword v20, v[18:19], off offset:512
	global_load_dword v21, v[16:17], off offset:512
	s_lshl_b32 s2, s6, 2
	s_add_i32 s2, s2, 0
	s_add_i32 s2, s2, 0x21660
	v_mov_b32_e32 v16, s2
	s_waitcnt vmcnt(0)
	ds_read_b32 v17, v16
	v_lshlrev_b32_e32 v3, 12, v3
	v_lshlrev_b32_e32 v5, 12, v5
	v_lshlrev_b32_e32 v16, 12, v21
	v_lshlrev_b32_e32 v18, 12, v20
	s_waitcnt lgkmcnt(0)
	v_cmp_lt_i32_e32 vcc, v2, v17
	s_nop 1
	v_cndmask_b32_e32 v3, 0, v3, vcc
	v_cmp_lt_i32_e32 vcc, v4, v17
	s_nop 1
	v_cndmask_b32_e32 v5, 0, v5, vcc
	v_cmp_lt_i32_e32 vcc, v14, v17
	s_nop 1
	v_cndmask_b32_e32 v16, 0, v16, vcc
	v_cmp_lt_i32_e32 vcc, v15, v17
	s_nop 1
	v_cndmask_b32_e32 v17, 0, v18, vcc
	s_cbranch_execz .LBB0_1081
	s_branch .LBB0_1082

; __device__ __forceinline__ unsigned cvt_pk_bf16(float lo, float hi) { unsigned r; asm volatile("v_cvt_pk_bf16_f32 %0, %1, %2" : "=v"(r) : "v"(lo), "v"(hi)); return r; }
; #define PG8_STAGE(bufoff, gbase, v0, v1) do { \
;         __builtin_amdgcn_global_load_lds((const unsigned*)((const char*)(gbase) + (v0)), (LAS unsigned*)(lds + (bufoff) + ldsw), 16, 0, 0); \
;         __builtin_amdgcn_global_load_lds((const unsigned*)((const char*)(gbase) + (v1)), (LAS unsigned*)(lds + (bufoff) + ldsw + 8192), 16, 0, 0); } while (0)
; #define PG8_LDA(dst, b, h) do { _Pragma("unroll") for (int m = 0; m < 4; ++m) _Pragma("unroll") for (int k = 0; k < 2; ++k) dst[m][k] = *(const LAS bf16x8*)(lds + PG8_SA(b, h) + aoff + m * 2048 + k * 1024); } while (0)
; #define PG8_WAIT_V(n) asm volatile("s_waitcnt vmcnt(" #n ")" ::: "memory")
; #define PG8_WAIT_L(n) asm volatile("s_waitcnt lgkmcnt(" #n ")" ::: "memory")
; #define PG8_BAR __builtin_amdgcn_s_barrier()
; template <class Epi, class Sched>
; __device__ __forceinline__ void gemm_phase(LAS unsigned char* lds, const int K, const Sched& S, const Epi& E) {
;     ...
;             PG8_LDB(B0, 0, 0); PG8_SCHED; PG8_LDA(At, 0, 0); PG8_STAGE(PG8_SA(1, 1), a1, c10, c11);
;             PG8_WAIT_L(8); PG8_BAR; PG8_WAIT_L(0); PG8_MMA(0, 0, At, B0); PG8_BAR; PG8_SCHED;
;             PG8_LDB(B1, 0, 1); PG8_STAGE(PG8_SB(0, 0), b2, voffB0, voffB1);
;             PG8_BAR; PG8_WAIT_L(0); PG8_MMA(0, 1, At, B1); PG8_BAR;
;             PG8_LDA(At, 0, 1); PG8_STAGE(PG8_SA(0, 0), a2, x00, x01);
;             PG8_BAR; PG8_WAIT_L(0); PG8_MMA(1, 0, At, B0); PG8_BAR; PG8_SCHED;
;             PG8_STAGE(PG8_SB(0, 1), b2 + hstep, voffB0, voffB1);
;             PG8_WAIT_V(6); PG8_BAR; PG8_MMA(1, 1, At, B1); PG8_BAR;
; template <int BANK, int WAITN> __device__ __forceinline__ void bg_finish1(BgState& b) {
;     ...
;         for (int c = 0; c < 4; ++c) { u32x4 w;
;             w.x = cvt_pk_bf16(b.r[(BANK * 8 + 0) * 4 + c], b.r[(BANK * 8 + 1) * 4 + c]); w.y = cvt_pk_bf16(b.r[(BANK * 8 + 2) * 4 + c], b.r[(BANK * 8 + 3) * 4 + c]);
;             w.z = cvt_pk_bf16(b.r[(BANK * 8 + 4) * 4 + c], b.r[(BANK * 8 + 5) * 4 + c]); w.w = cvt_pk_bf16(b.r[(BANK * 8 + 6) * 4 + c], b.r[(BANK * 8 + 7) * 4 + c]);
;             bf16_t* dp = dst + (c & 1) * 512 + (c >> 1) * b.o2[BANK];
;             asm volatile("global_store_dwordx4 %0, %1, off\n\ts_nop 1" :: "v"(dp), "v"(w) : "memory"); }
.LBB0_1094:
	v_add_u32_e32 v139, s46, v149
	s_add_u32 s22, s0, s20
	ds_read_b128 v[160:163], v139
	ds_read_b128 v[164:167], v139 offset:1024
	ds_read_b128 v[168:171], v139 offset:2048
	ds_read_b128 v[172:175], v139 offset:3072
	s_addc_u32 s23, s1, s21
	s_add_u32 s24, s22, 0x34c30100
	s_addc_u32 s25, s23, 0
	s_cmpk_eq_i32 s20, 0xf00
	s_cselect_b64 vcc, -1, 0
	s_and_b64 s[22:23], vcc, exec
	v_cndmask_b32_e32 v134, v158, v156, vcc
	s_cselect_b32 s27, s3, s25
	s_cselect_b32 s26, s2, s24
	v_cndmask_b32_e32 v139, v138, v154, vcc
	s_cselect_b32 s23, s19, s15
	s_cselect_b32 s22, s18, s13
	v_cndmask_b32_e32 v204, v136, v155, vcc
	s_add_u32 s24, s22, 0x20000
	s_addc_u32 s25, s23, 0
	v_lshl_add_u64 v[206:207], v[144:145], 0, s[20:21]
	s_add_i32 m0, s37, 0xc000
	ds_read_b128 v[176:179], v151
	ds_read_b128 v[180:183], v151 offset:1024
	ds_read_b128 v[184:187], v151 offset:2048
	ds_read_b128 v[188:191], v151 offset:3072
	ds_read_b128 v[192:195], v151 offset:4096
	ds_read_b128 v[196:199], v151 offset:5120
	ds_read_b128 v[200:203], v151 offset:6144
	ds_read_b128 v[208:211], v151 offset:7168
	global_load_lds_dwordx4 v[206:207], off
	v_lshl_add_u64 v[206:207], v[142:143], 0, s[20:21]
	s_add_i32 m0, s37, 0xe000
	s_nop 0
	global_load_lds_dwordx4 v[206:207], off
	s_waitcnt lgkmcnt(8)
	s_barrier
	s_waitcnt lgkmcnt(0)
	s_setprio 1
	s_waitcnt lgkmcnt(0)
	v_mfma_f32_16x16x32_bf16 v[126:129], v[160:163], v[176:179], v[126:129]
	v_mfma_f32_16x16x32_bf16 v[122:125], v[168:171], v[176:179], v[122:125]
	v_mfma_f32_16x16x32_bf16 v[110:113], v[160:163], v[184:187], v[110:113]
	v_mfma_f32_16x16x32_bf16 v[106:109], v[168:171], v[184:187], v[106:109]
	v_mfma_f32_16x16x32_bf16 v[94:97], v[160:163], v[192:195], v[94:97]
	v_mfma_f32_16x16x32_bf16 v[90:93], v[168:171], v[192:195], v[90:93]
	v_mfma_f32_16x16x32_bf16 v[78:81], v[160:163], v[200:203], v[78:81]
	v_mfma_f32_16x16x32_bf16 v[74:77], v[168:171], v[200:203], v[74:77]
	v_mfma_f32_16x16x32_bf16 v[126:129], v[164:167], v[180:183], v[126:129]
	v_mfma_f32_16x16x32_bf16 v[122:125], v[172:175], v[180:183], v[122:125]
	v_mfma_f32_16x16x32_bf16 v[110:113], v[164:167], v[188:191], v[110:113]
	v_mfma_f32_16x16x32_bf16 v[106:109], v[172:175], v[188:191], v[106:109]
	v_mfma_f32_16x16x32_bf16 v[94:97], v[164:167], v[196:199], v[94:97]
	v_mfma_f32_16x16x32_bf16 v[90:93], v[172:175], v[196:199], v[90:93]
	v_mfma_f32_16x16x32_bf16 v[78:81], v[164:167], v[208:211], v[78:81]
	v_mfma_f32_16x16x32_bf16 v[74:77], v[172:175], v[208:211], v[74:77]
	s_setprio 0
	s_barrier
	s_add_i32 s55, s46, s36
	v_add_u32_e32 v141, s48, v149
	v_lshl_add_u64 v[206:207], s[22:23], 0, v[130:131]
	s_mov_b32 m0, s55
	ds_read_b128 v[212:215], v141
	ds_read_b128 v[216:219], v141 offset:1024
	ds_read_b128 v[220:223], v141 offset:2048
	ds_read_b128 v[224:227], v141 offset:3072
	global_load_lds_dwordx4 v[206:207], off
	v_lshl_add_u64 v[228:229], s[22:23], 0, v[132:133]
	s_add_i32 m0, s55, 0x2000
	s_nop 0
	global_load_lds_dwordx4 v[228:229], off
	s_barrier
	s_waitcnt lgkmcnt(0)
	s_setprio 1
	s_waitcnt lgkmcnt(0)
	v_mfma_f32_16x16x32_bf16 v[118:121], v[212:215], v[176:179], v[118:121]
	v_mfma_f32_16x16x32_bf16 v[114:117], v[220:223], v[176:179], v[114:117]
	v_mfma_f32_16x16x32_bf16 v[102:105], v[212:215], v[184:187], v[102:105]
	v_mfma_f32_16x16x32_bf16 v[98:101], v[220:223], v[184:187], v[98:101]
	v_mfma_f32_16x16x32_bf16 v[86:89], v[212:215], v[192:195], v[86:89]
	v_mfma_f32_16x16x32_bf16 v[82:85], v[220:223], v[192:195], v[82:85]
	v_mfma_f32_16x16x32_bf16 v[70:73], v[212:215], v[200:203], v[70:73]
	v_mfma_f32_16x16x32_bf16 v[66:69], v[220:223], v[200:203], v[66:69]
	v_mfma_f32_16x16x32_bf16 v[118:121], v[216:219], v[180:183], v[118:121]
	v_mfma_f32_16x16x32_bf16 v[114:117], v[224:227], v[180:183], v[114:117]
	v_mfma_f32_16x16x32_bf16 v[102:105], v[216:219], v[188:191], v[102:105]
	v_mfma_f32_16x16x32_bf16 v[98:101], v[224:227], v[188:191], v[98:101]
	v_mfma_f32_16x16x32_bf16 v[86:89], v[216:219], v[196:199], v[86:89]
	v_mfma_f32_16x16x32_bf16 v[82:85], v[224:227], v[196:199], v[82:85]
	v_mfma_f32_16x16x32_bf16 v[70:73], v[216:219], v[208:211], v[70:73]
	v_mfma_f32_16x16x32_bf16 v[66:69], v[224:227], v[208:211], v[66:69]
	s_setprio 0
	s_mov_b32 m0, s37
	s_barrier
	ds_read_b128 v[176:179], v151 offset:16384
	ds_read_b128 v[180:183], v151 offset:17408
	ds_read_b128 v[184:187], v151 offset:18432
	ds_read_b128 v[188:191], v151 offset:19456
	ds_read_b128 v[192:195], v151 offset:20480
	ds_read_b128 v[196:199], v151 offset:21504
	ds_read_b128 v[200:203], v151 offset:22528
	ds_read_b128 v[208:211], v151 offset:23552
	global_load_lds_dwordx4 v134, s[26:27]
	s_mov_b32 m0, s38
	v_mov_b32_e32 v205, v135
	global_load_lds_dwordx4 v204, s[26:27]
	s_barrier
	s_waitcnt lgkmcnt(0)
	v_lshl_add_u64 v[230:231], s[26:27], 0, v[134:135]
	v_lshl_add_u64 v[204:205], s[26:27], 0, v[204:205]
	s_setprio 1
	s_waitcnt lgkmcnt(0)
	v_mfma_f32_16x16x32_bf16 v[62:65], v[160:163], v[176:179], v[62:65]
	v_mfma_f32_16x16x32_bf16 v[58:61], v[168:171], v[176:179], v[58:61]
	v_mfma_f32_16x16x32_bf16 v[46:49], v[160:163], v[184:187], v[46:49]
	v_mfma_f32_16x16x32_bf16 v[42:45], v[168:171], v[184:187], v[42:45]
	v_mfma_f32_16x16x32_bf16 v[30:33], v[160:163], v[192:195], v[30:33]
	v_mfma_f32_16x16x32_bf16 v[26:29], v[168:171], v[192:195], v[26:29]
	v_mfma_f32_16x16x32_bf16 v[14:17], v[160:163], v[200:203], v[14:17]
	v_mfma_f32_16x16x32_bf16 v[10:13], v[168:171], v[200:203], v[10:13]
	v_mfma_f32_16x16x32_bf16 v[62:65], v[164:167], v[180:183], v[62:65]
	v_mfma_f32_16x16x32_bf16 v[58:61], v[172:175], v[180:183], v[58:61]
	v_mfma_f32_16x16x32_bf16 v[46:49], v[164:167], v[188:191], v[46:49]
	v_mfma_f32_16x16x32_bf16 v[42:45], v[172:175], v[188:191], v[42:45]
	v_mfma_f32_16x16x32_bf16 v[30:33], v[164:167], v[196:199], v[30:33]
	v_mfma_f32_16x16x32_bf16 v[26:29], v[172:175], v[196:199], v[26:29]
	v_mfma_f32_16x16x32_bf16 v[14:17], v[164:167], v[208:211], v[14:17]
	v_mfma_f32_16x16x32_bf16 v[10:13], v[172:175], v[208:211], v[10:13]
	s_setprio 0
	s_barrier
	s_add_i32 s55, s48, s36
	v_lshl_add_u64 v[160:161], v[206:207], 0, s[4:5]
	s_mov_b32 m0, s55
	s_nop 0
	global_load_lds_dwordx4 v[160:161], off
	v_lshl_add_u64 v[160:161], v[228:229], 0, s[4:5]
	s_add_i32 m0, s55, 0x2000
	s_nop 0
	global_load_lds_dwordx4 v[160:161], off
	s_cmp_eq_u32 s82, 0
	s_cbranch_scc1 .Lpb8_p4n
	s_waitcnt vmcnt(8)
	v_cvt_pk_bf16_f32 v244, v244, v245
	v_cvt_pk_bf16_f32 v245, v246, v247
	v_cvt_pk_bf16_f32 v246, v248, v249
	v_cvt_pk_bf16_f32 v247, v250, v251
	global_store_dwordx4 v253, v[244:247], s[78:79]
	s_mov_b32 s82, 0
	s_waitcnt vmcnt(7)
	s_branch .Lpb8_p4j
; #define PG8_STAGE(bufoff, gbase, v0, v1) do { \
;         __builtin_amdgcn_global_load_lds((const unsigned*)((const char*)(gbase) + (v0)), (LAS unsigned*)(lds + (bufoff) + ldsw), 16, 0, 0); \
;         __builtin_amdgcn_global_load_lds((const unsigned*)((const char*)(gbase) + (v1)), (LAS unsigned*)(lds + (bufoff) + ldsw + 8192), 16, 0, 0); } while (0)
; #define PG8_LDA(dst, b, h) do { _Pragma("unroll") for (int m = 0; m < 4; ++m) _Pragma("unroll") for (int k = 0; k < 2; ++k) dst[m][k] = *(const LAS bf16x8*)(lds + PG8_SA(b, h) + aoff + m * 2048 + k * 1024); } while (0)
; #define PG8_LDB(dst, b, h) do { _Pragma("unroll") for (int n = 0; n < 2; ++n) _Pragma("unroll") for (int k = 0; k < 2; ++k) dst[n][k] = *(const LAS bf16x8*)(lds + PG8_SB(b, h) + boff + n * 2048 + k * 1024); } while (0)
; #define PG8_MMA(ai, bj, At, Bt) do { __builtin_amdgcn_s_setprio(1); _Pragma("unroll") for (int m = 0; m < 4; ++m) _Pragma("unroll") for (int n = 0; n < 2; ++n) _Pragma("unroll") for (int k = 0; k < 2; ++k) \
;         acc[ai][bj][m][n] = __builtin_amdgcn_mfma_f32_16x16x32_bf16(Bt[n][k], At[m][k], acc[ai][bj][m][n], 0, 0, 0); __builtin_amdgcn_s_setprio(0); } while (0)
; #define PG8_WAIT_V(n) asm volatile("s_waitcnt vmcnt(" #n ")" ::: "memory")
; #define PG8_WAIT_L(n) asm volatile("s_waitcnt lgkmcnt(" #n ")" ::: "memory")
; #define PG8_BAR __builtin_amdgcn_s_barrier()
; #define PG8_SCHED __builtin_amdgcn_sched_barrier(0)
; template <class Epi, class Sched>
; __device__ __forceinline__ void gemm_phase(LAS unsigned char* lds, const int K, const Sched& S, const Epi& E) {
;     ...
;             PG8_WAIT_V(6); PG8_BAR; PG8_MMA(1, 1, At, B1); PG8_BAR;
;             PG8_LDB(B0, 1, 0); PG8_SCHED; PG8_LDA(At, 1, 0); PG8_STAGE(PG8_SA(0, 1), a2, x10, x11);
;             PG8_WAIT_L(8); PG8_BAR; PG8_WAIT_L(0); PG8_MMA(0, 0, At, B0); PG8_BAR; PG8_SCHED;
;             PG8_LDB(B1, 1, 1); PG8_STAGE(PG8_SB(1, 0), b3, voffB0, voffB1);
;             PG8_BAR; PG8_WAIT_L(0); PG8_MMA(0, 1, At, B1); PG8_BAR;
;             PG8_LDA(At, 1, 1); PG8_STAGE(PG8_SA(1, 0), a3, x00, x01);
;             PG8_BAR; PG8_WAIT_L(0); PG8_MMA(1, 0, At, B0); PG8_BAR; PG8_SCHED;
.Lpb8_p4n:
	s_waitcnt vmcnt(6)
.Lpb8_p4j:
	s_barrier
	s_setprio 1
	v_mfma_f32_16x16x32_bf16 v[54:57], v[212:215], v[176:179], v[54:57]
	v_mfma_f32_16x16x32_bf16 v[50:53], v[220:223], v[176:179], v[50:53]
	v_mfma_f32_16x16x32_bf16 v[38:41], v[212:215], v[184:187], v[38:41]
	v_mfma_f32_16x16x32_bf16 v[34:37], v[220:223], v[184:187], v[34:37]
	v_mfma_f32_16x16x32_bf16 v[22:25], v[212:215], v[192:195], v[22:25]
	v_mfma_f32_16x16x32_bf16 v[18:21], v[220:223], v[192:195], v[18:21]
	v_mfma_f32_16x16x32_bf16 v[6:9], v[212:215], v[200:203], v[6:9]
	v_mfma_f32_16x16x32_bf16 v[2:5], v[220:223], v[200:203], v[2:5]
	v_mfma_f32_16x16x32_bf16 v[54:57], v[216:219], v[180:183], v[54:57]
	v_mfma_f32_16x16x32_bf16 v[50:53], v[224:227], v[180:183], v[50:53]
	v_mfma_f32_16x16x32_bf16 v[38:41], v[216:219], v[188:191], v[38:41]
	v_mfma_f32_16x16x32_bf16 v[34:37], v[224:227], v[188:191], v[34:37]
	v_mfma_f32_16x16x32_bf16 v[22:25], v[216:219], v[196:199], v[22:25]
	v_mfma_f32_16x16x32_bf16 v[18:21], v[224:227], v[196:199], v[18:21]
	v_mfma_f32_16x16x32_bf16 v[6:9], v[216:219], v[208:211], v[6:9]
	v_mfma_f32_16x16x32_bf16 v[2:5], v[224:227], v[208:211], v[2:5]
	s_setprio 0
	s_add_i32 s55, 0, 0x18000
	v_add_u32_e32 v134, s55, v149
	s_barrier
	ds_read_b128 v[160:163], v134
	ds_read_b128 v[164:167], v134 offset:1024
	ds_read_b128 v[168:171], v134 offset:2048
	ds_read_b128 v[172:175], v134 offset:3072
	s_mov_b32 m0, s39
	ds_read_b128 v[176:179], v151 offset:32768
	ds_read_b128 v[180:183], v151 offset:33792
	ds_read_b128 v[184:187], v151 offset:34816
	ds_read_b128 v[188:191], v151 offset:35840
	ds_read_b128 v[192:195], v151 offset:36864
	ds_read_b128 v[196:199], v151 offset:37888
	ds_read_b128 v[200:203], v151 offset:38912
	ds_read_b128 v[208:211], v151 offset:39936
	v_cndmask_b32_e32 v134, v140, v153, vcc
	global_load_lds_dwordx4 v139, s[26:27]
	s_mov_b32 m0, s40
	s_nop 0
	global_load_lds_dwordx4 v134, s[26:27]
	s_waitcnt lgkmcnt(8)
	s_barrier
	s_waitcnt lgkmcnt(0)
	s_setprio 1
	s_waitcnt lgkmcnt(0)
	v_mfma_f32_16x16x32_bf16 v[126:129], v[160:163], v[176:179], v[126:129]
	v_mfma_f32_16x16x32_bf16 v[122:125], v[168:171], v[176:179], v[122:125]
	v_mfma_f32_16x16x32_bf16 v[110:113], v[160:163], v[184:187], v[110:113]
	v_mfma_f32_16x16x32_bf16 v[106:109], v[168:171], v[184:187], v[106:109]
	v_mfma_f32_16x16x32_bf16 v[94:97], v[160:163], v[192:195], v[94:97]
	v_mfma_f32_16x16x32_bf16 v[90:93], v[168:171], v[192:195], v[90:93]
	v_mfma_f32_16x16x32_bf16 v[78:81], v[160:163], v[200:203], v[78:81]
	v_mfma_f32_16x16x32_bf16 v[74:77], v[168:171], v[200:203], v[74:77]
	v_mfma_f32_16x16x32_bf16 v[126:129], v[164:167], v[180:183], v[126:129]
	v_mfma_f32_16x16x32_bf16 v[122:125], v[172:175], v[180:183], v[122:125]
	v_mfma_f32_16x16x32_bf16 v[110:113], v[164:167], v[188:191], v[110:113]
	v_mfma_f32_16x16x32_bf16 v[106:109], v[172:175], v[188:191], v[106:109]
	v_mfma_f32_16x16x32_bf16 v[94:97], v[164:167], v[196:199], v[94:97]
	v_mfma_f32_16x16x32_bf16 v[90:93], v[172:175], v[196:199], v[90:93]
	v_mfma_f32_16x16x32_bf16 v[78:81], v[164:167], v[208:211], v[78:81]
	v_mfma_f32_16x16x32_bf16 v[74:77], v[172:175], v[208:211], v[74:77]
	s_setprio 0
	s_barrier
	s_add_i32 s26, 0, 0x1c000
	s_add_i32 s27, s55, s36
	v_add_u32_e32 v134, s26, v149
	v_lshl_add_u64 v[206:207], s[24:25], 0, v[130:131]
	s_mov_b32 m0, s27
	ds_read_b128 v[212:215], v134
	ds_read_b128 v[216:219], v134 offset:1024
	ds_read_b128 v[220:223], v134 offset:2048
	ds_read_b128 v[224:227], v134 offset:3072
	global_load_lds_dwordx4 v[206:207], off
	v_lshl_add_u64 v[206:207], s[24:25], 0, v[132:133]
	s_add_i32 m0, s27, 0x2000
	s_nop 0
	global_load_lds_dwordx4 v[206:207], off
	s_barrier
; #define PG8_STAGE(bufoff, gbase, v0, v1) do { \
;         __builtin_amdgcn_global_load_lds((const unsigned*)((const char*)(gbase) + (v0)), (LAS unsigned*)(lds + (bufoff) + ldsw), 16, 0, 0); \
;         __builtin_amdgcn_global_load_lds((const unsigned*)((const char*)(gbase) + (v1)), (LAS unsigned*)(lds + (bufoff) + ldsw + 8192), 16, 0, 0); } while (0)
; #define PG8_LDA(dst, b, h) do { _Pragma("unroll") for (int m = 0; m < 4; ++m) _Pragma("unroll") for (int k = 0; k < 2; ++k) dst[m][k] = *(const LAS bf16x8*)(lds + PG8_SA(b, h) + aoff + m * 2048 + k * 1024); } while (0)
; #define PG8_MMA(ai, bj, At, Bt) do { __builtin_amdgcn_s_setprio(1); _Pragma("unroll") for (int m = 0; m < 4; ++m) _Pragma("unroll") for (int n = 0; n < 2; ++n) _Pragma("unroll") for (int k = 0; k < 2; ++k) \
;         acc[ai][bj][m][n] = __builtin_amdgcn_mfma_f32_16x16x32_bf16(Bt[n][k], At[m][k], acc[ai][bj][m][n], 0, 0, 0); __builtin_amdgcn_s_setprio(0); } while (0)
; #define PG8_WAIT_V(n) asm volatile("s_waitcnt vmcnt(" #n ")" ::: "memory")
; #define PG8_WAIT_L(n) asm volatile("s_waitcnt lgkmcnt(" #n ")" ::: "memory")
; #define PG8_BAR __builtin_amdgcn_s_barrier()
; #define PG8_SCHED __builtin_amdgcn_sched_barrier(0)
; template <class Epi, class Sched>
; __device__ __forceinline__ void gemm_phase(LAS unsigned char* lds, const int K, const Sched& S, const Epi& E) {
;     ...
;             PG8_BAR; PG8_WAIT_L(0); PG8_MMA(0, 1, At, B1); PG8_BAR;
;             PG8_LDA(At, 1, 1); PG8_STAGE(PG8_SA(1, 0), a3, x00, x01);
;             PG8_BAR; PG8_WAIT_L(0); PG8_MMA(1, 0, At, B0); PG8_BAR; PG8_SCHED;
;             PG8_STAGE(PG8_SB(1, 1), b3 + hstep, voffB0, voffB1);
;             PG8_WAIT_V(6); PG8_BAR; PG8_MMA(1, 1, At, B1); PG8_BAR;
; __device__ __forceinline__ bool bg_decode(int st, int wg, int NW, int lane, KP kp, const float*& src, int& ldS, bf16_t*& dst, int& o2) {
;     ...
;     if (r < 65536) {
;         const int e = r >> 10, kc = (r >> 2) & 255, kind = (r >> 1) & 1, cc = r & 1, n = cc * 256 + lane;
;         ldS = FF; o2 = 256 * 8;
;         src = kp->in[27 + kind] + ((size_t)(l * NE + e) * D + kc * 8) * FF + n;
;         const int drow = (n >> 7) * 256 + kind * 128 + (n & 127);
;         dst = (bf16_t*)(ws + WS_WGU) + l * WGU_L + (size_t)e * 1024 * D + ((size_t)kc * 1024 + drow) * 8;
	s_waitcnt lgkmcnt(0)
	s_setprio 1
	s_waitcnt lgkmcnt(0)
	v_mfma_f32_16x16x32_bf16 v[118:121], v[212:215], v[176:179], v[118:121]
	v_mfma_f32_16x16x32_bf16 v[114:117], v[220:223], v[176:179], v[114:117]
	v_mfma_f32_16x16x32_bf16 v[102:105], v[212:215], v[184:187], v[102:105]
	v_mfma_f32_16x16x32_bf16 v[98:101], v[220:223], v[184:187], v[98:101]
	v_mfma_f32_16x16x32_bf16 v[86:89], v[212:215], v[192:195], v[86:89]
	v_mfma_f32_16x16x32_bf16 v[82:85], v[220:223], v[192:195], v[82:85]
	v_mfma_f32_16x16x32_bf16 v[70:73], v[212:215], v[200:203], v[70:73]
	v_mfma_f32_16x16x32_bf16 v[66:69], v[220:223], v[200:203], v[66:69]
	v_mfma_f32_16x16x32_bf16 v[118:121], v[216:219], v[180:183], v[118:121]
	v_mfma_f32_16x16x32_bf16 v[114:117], v[224:227], v[180:183], v[114:117]
	v_mfma_f32_16x16x32_bf16 v[102:105], v[216:219], v[188:191], v[102:105]
	v_mfma_f32_16x16x32_bf16 v[98:101], v[224:227], v[188:191], v[98:101]
	v_mfma_f32_16x16x32_bf16 v[86:89], v[216:219], v[196:199], v[86:89]
	v_mfma_f32_16x16x32_bf16 v[82:85], v[224:227], v[196:199], v[82:85]
	v_mfma_f32_16x16x32_bf16 v[70:73], v[216:219], v[208:211], v[70:73]
	v_mfma_f32_16x16x32_bf16 v[66:69], v[224:227], v[208:211], v[66:69]
	s_setprio 0
	s_mov_b32 m0, s43
	v_lshl_add_u64 v[206:207], v[230:231], 0, s[10:11]
	s_barrier
	ds_read_b128 v[176:179], v151 offset:49152
	ds_read_b128 v[180:183], v151 offset:50176
	ds_read_b128 v[184:187], v151 offset:51200
	ds_read_b128 v[188:191], v151 offset:52224
	ds_read_b128 v[192:195], v151 offset:53248
	ds_read_b128 v[196:199], v151 offset:54272
	ds_read_b128 v[200:203], v151 offset:55296
	ds_read_b128 v[208:211], v151 offset:56320
	global_load_lds_dwordx4 v[206:207], off
	v_lshl_add_u64 v[204:205], v[204:205], 0, s[10:11]
	s_mov_b32 m0, s44
	s_nop 0
	global_load_lds_dwordx4 v[204:205], off
	s_barrier
	s_waitcnt lgkmcnt(0)
	s_setprio 1
	s_waitcnt lgkmcnt(0)
	v_mfma_f32_16x16x32_bf16 v[62:65], v[160:163], v[176:179], v[62:65]
	v_mfma_f32_16x16x32_bf16 v[58:61], v[168:171], v[176:179], v[58:61]
	v_mfma_f32_16x16x32_bf16 v[46:49], v[160:163], v[184:187], v[46:49]
	v_mfma_f32_16x16x32_bf16 v[42:45], v[168:171], v[184:187], v[42:45]
	v_mfma_f32_16x16x32_bf16 v[30:33], v[160:163], v[192:195], v[30:33]
	v_mfma_f32_16x16x32_bf16 v[26:29], v[168:171], v[192:195], v[26:29]
	v_mfma_f32_16x16x32_bf16 v[14:17], v[160:163], v[200:203], v[14:17]
	v_mfma_f32_16x16x32_bf16 v[10:13], v[168:171], v[200:203], v[10:13]
	v_mfma_f32_16x16x32_bf16 v[62:65], v[164:167], v[180:183], v[62:65]
	v_mfma_f32_16x16x32_bf16 v[58:61], v[172:175], v[180:183], v[58:61]
	v_mfma_f32_16x16x32_bf16 v[46:49], v[164:167], v[188:191], v[46:49]
	v_mfma_f32_16x16x32_bf16 v[42:45], v[172:175], v[188:191], v[42:45]
	v_mfma_f32_16x16x32_bf16 v[30:33], v[164:167], v[196:199], v[30:33]
	v_mfma_f32_16x16x32_bf16 v[26:29], v[172:175], v[196:199], v[26:29]
	v_mfma_f32_16x16x32_bf16 v[14:17], v[164:167], v[208:211], v[14:17]
	v_mfma_f32_16x16x32_bf16 v[10:13], v[172:175], v[208:211], v[10:13]
	s_setprio 0
	s_barrier
	s_add_u32 s22, s22, 0x20800
	s_addc_u32 s23, s23, 0
	s_add_i32 s24, s26, s36
	v_lshl_add_u64 v[160:161], s[22:23], 0, v[130:131]
	s_mov_b32 m0, s24
	s_nop 0
	global_load_lds_dwordx4 v[160:161], off
	v_lshl_add_u64 v[160:161], s[22:23], 0, v[132:133]
	s_add_i32 m0, s24, 0x2000
	s_nop 0
	global_load_lds_dwordx4 v[160:161], off
	s_cmp_ge_u32 s70, 0x28000
	s_cbranch_scc1 .Lpb8_p8n
	s_cmp_eq_u32 s80, 0
	s_cbranch_scc0 .Lpb8_adv2
	s_cmp_ge_u32 s70, 0x18000
	s_cselect_b32 s84, 0x18000, 0
	s_cselect_b32 s83, 0x10000000, 0
	s_mov_b32 s81, 0x4030000
	s_cselect_b32 s81, 0x14430000, s81
	s_sub_u32 s84, s70, s84
	s_lshr_b32 s85, s84, 2
	s_lshl_b32 s85, s85, 14
	s_and_b32 s86, s84, 1
	s_lshl_b32 s87, s86, 10
	s_add_u32 s87, s87, s85
	s_add_u32 s87, s87, s83
	s_bitcmp1_b32 s84, 1
	s_cselect_b64 s[72:73], s[76:77], s[74:75]
	s_add_u32 s72, s72, s87
	s_addc_u32 s73, s73, 0
	s_add_u32 s88, s72, 0x2000
	s_addc_u32 s89, s73, 0
	s_lshl_b32 s86, s86, 13
	s_add_u32 s85, s85, s86
	s_and_b32 s86, s84, 2
	s_lshl_b32 s86, s86, 10
	s_add_u32 s85, s85, s86
	s_add_u32 s85, s85, s81
	v_add_u32_e32 v253, s85, v252
	s_movk_i32 s81, 0x400
	s_branch .Lpb8_ld2
.Lpb8_adv2:
	v_add_u32_e32 v253, s81, v253
	s_xor_b32 s81, s81, 0x800
	s_add_u32 s72, s72, 0x100
	s_addc_u32 s73, s73, 0
	s_add_u32 s88, s88, 0x100
	s_addc_u32 s89, s89, 0
.Lpb8_ld2:
	global_load_dword v244, v238, s[72:73]
	global_load_dword v245, v239, s[72:73]
	global_load_dword v246, v240, s[72:73]
	global_load_dword v247, v241, s[72:73]
	global_load_dword v248, v238, s[88:89]
	global_load_dword v249, v239, s[88:89]
	global_load_dword v250, v240, s[88:89]
	global_load_dword v251, v241, s[88:89]
	s_add_u32 s80, s80, 1
	s_and_b32 s80, s80, 3
	s_cmp_eq_u32 s80, 0
	s_cselect_b32 s84, s71, 0
	s_add_u32 s70, s70, s84
	s_mov_b32 s82, 1
	s_waitcnt vmcnt(14)
	s_branch .Lpb8_p8j

; __device__ __forceinline__ unsigned cvt_pk_bf16(float lo, float hi) { unsigned r; asm volatile("v_cvt_pk_bf16_f32 %0, %1, %2" : "=v"(r) : "v"(lo), "v"(hi)); return r; }
; __device__ __forceinline__ bool bg_decode(int st, int wg, int NW, int lane, KP kp, const float*& src, int& ldS, bf16_t*& dst, int& o2) {
;     ...
;     if (r < 65536) {
;         const int e = r >> 10, kc = (r >> 2) & 255, kind = (r >> 1) & 1, cc = r & 1, n = cc * 256 + lane;
;         ldS = FF; o2 = 256 * 8;
;         src = kp->in[27 + kind] + ((size_t)(l * NE + e) * D + kc * 8) * FF + n;
;         const int drow = (n >> 7) * 256 + kind * 128 + (n & 127);
;         dst = (bf16_t*)(ws + WS_WGU) + l * WGU_L + (size_t)e * 1024 * D + ((size_t)kc * 1024 + drow) * 8;
; template <int BANK, int WAITN> __device__ __forceinline__ void bg_finish1(BgState& b) {
;     ...
;         for (int c = 0; c < 4; ++c) { u32x4 w;
;             w.x = cvt_pk_bf16(b.r[(BANK * 8 + 0) * 4 + c], b.r[(BANK * 8 + 1) * 4 + c]); w.y = cvt_pk_bf16(b.r[(BANK * 8 + 2) * 4 + c], b.r[(BANK * 8 + 3) * 4 + c]);
;             w.z = cvt_pk_bf16(b.r[(BANK * 8 + 4) * 4 + c], b.r[(BANK * 8 + 5) * 4 + c]); w.w = cvt_pk_bf16(b.r[(BANK * 8 + 6) * 4 + c], b.r[(BANK * 8 + 7) * 4 + c]);
;             bf16_t* dp = dst + (c & 1) * 512 + (c >> 1) * b.o2[BANK];
;             asm volatile("global_store_dwordx4 %0, %1, off\n\ts_nop 1" :: "v"(dp), "v"(w) : "memory"); }
.LBB0_1099:
.Lpb8_drain:
	s_cmp_eq_u32 s82, 0
	s_cbranch_scc1 .Lpb8_d1
	s_waitcnt vmcnt(0)
	v_cvt_pk_bf16_f32 v244, v244, v245
	v_cvt_pk_bf16_f32 v245, v246, v247
	v_cvt_pk_bf16_f32 v246, v248, v249
	v_cvt_pk_bf16_f32 v247, v250, v251
	global_store_dwordx4 v253, v[244:247], s[78:79]
	s_mov_b32 s82, 0
.Lpb8_d1:
	s_cmp_ge_u32 s70, 0x28000
	s_cbranch_scc1 .Lpb8_dend
	s_cmp_eq_u32 s80, 0
	s_cbranch_scc0 .Lpb8_adv1
	s_cmp_ge_u32 s70, 0x18000
	s_cselect_b32 s84, 0x18000, 0
	s_cselect_b32 s83, 0x10000000, 0
	s_mov_b32 s81, 0x4030000
	s_cselect_b32 s81, 0x14430000, s81
	s_sub_u32 s84, s70, s84
	s_lshr_b32 s85, s84, 2
	s_lshl_b32 s85, s85, 14
	s_and_b32 s86, s84, 1
	s_lshl_b32 s87, s86, 10
	s_add_u32 s87, s87, s85
	s_add_u32 s87, s87, s83
	s_bitcmp1_b32 s84, 1
	s_cselect_b64 s[72:73], s[76:77], s[74:75]
	s_add_u32 s72, s72, s87
	s_addc_u32 s73, s73, 0
	s_add_u32 s88, s72, 0x2000
	s_addc_u32 s89, s73, 0
	s_lshl_b32 s86, s86, 13
	s_add_u32 s85, s85, s86
	s_and_b32 s86, s84, 2
	s_lshl_b32 s86, s86, 10
	s_add_u32 s85, s85, s86
	s_add_u32 s85, s85, s81
	v_add_u32_e32 v253, s85, v252
	s_movk_i32 s81, 0x400
	s_branch .Lpb8_ld1

; template <int BANK> __device__ __forceinline__ void bg_issue1(BgState& b, int wg, int NW, int lane) {
;     ...
;     for (int i = 0; i < 8; ++i) { const float* p = src + (size_t)i * ldS;
;         asm volatile("global_load_dword %0, %4, off\n\tglobal_load_dword %1, %4, off offset:256\n\tglobal_load_dword %2, %4, off offset:512\n\tglobal_load_dword %3, %4, off offset:768"
;                      : "=&v"(b.r[(BANK * 8 + i) * 4 + 0]), "=&v"(b.r[(BANK * 8 + i) * 4 + 1]), "=&v"(b.r[(BANK * 8 + i) * 4 + 2]), "=&v"(b.r[(BANK * 8 + i) * 4 + 3]) : "v"(p) : "memory"); }
;     b.st += 1;
; }
.Lpb8_ld1:
	global_load_dword v244, v238, s[72:73]
	global_load_dword v245, v239, s[72:73]
	global_load_dword v246, v240, s[72:73]
	global_load_dword v247, v241, s[72:73]
	global_load_dword v248, v238, s[88:89]
	global_load_dword v249, v239, s[88:89]
	global_load_dword v250, v240, s[88:89]
	global_load_dword v251, v241, s[88:89]
	s_add_u32 s80, s80, 1
	s_and_b32 s80, s80, 3
	s_cmp_eq_u32 s80, 0
	s_cselect_b32 s84, s71, 0
	s_add_u32 s70, s70, s84
	s_mov_b32 s82, 1
	s_branch .Lpb8_drain

; __device__ __forceinline__ int tid_fresh() { int t = threadIdx.x; asm volatile("" : "+v"(t)); return t; }
;     __device__ __forceinline__ void a_off4(const Unit& u, int r0, int r1, unsigned& o00, unsigned& o01, unsigned& o10, unsigned& o11) const { o00 = a_off(u, r0); o01 = a_off(u, r1); o10 = a_off(u, HALF + r0); o11 = a_off(u, HALF + r1); }
;     __device__ __forceinline__ unsigned b_off(int R, int C) const { return (unsigned)(R * K + C) * 2u; }
;     __device__ __forceinline__ size_t b_kstep() const { return (size_t)(BK * 2); }
;     __device__ __forceinline__ size_t b_hstep() const { return (size_t)HALF * 16; }
; template <class Epi, class Sched>
; __device__ __forceinline__ void gemm_phase(LAS unsigned char* lds, const int K, const Sched& S, const Epi& E) {
;     const int tid = tid_fresh(), wid = __builtin_amdgcn_readfirstlane(tid >> 6), lane = tid & 63, wr = wid >> 2, wc = wid & 3, fr = lane & 15, fq = lane >> 4;
;     const int nt = K / BK;
;     int R0, C0, R1, C1; stage_rc(tid * 16, R0, C0); stage_rc(tid * 16 + 8192, R1, C1);
;     const int Rb0 = Epi::PERM ? ((R0 & ~31) + perm32(R0 & 31)) : R0, Rb1 = Epi::PERM ? ((R1 & ~31) + perm32(R1 & 31)) : R1;
;     const unsigned voffB0 = S.b_off(Rb0, C0), voffB1 = S.b_off(Rb1, C1);
;     const size_t kstep = (size_t)(BK * 2);
;     const size_t kstepB = S.b_kstep(), hstep = S.b_hstep();
;     const unsigned ldsw = (unsigned)wid * 1024u;
;     const int aoff = lds_byte(wr * 64 + fr, fq * 8), boff = lds_byte(wc * 32 + fr, fq * 8);
;     __device__ __forceinline__ void a_off4(const Unit& u, int r0, int r1, unsigned& o00, unsigned& o01, unsigned& o10, unsigned& o11) const {
;         const int p0 = u.pm * BM + r0, p1 = u.pm * BM + r1, p2 = p0 + HALF, p3 = p1 + HALF;
;         if (u.e >= NE) { o00 = (unsigned)p0 * (unsigned)(D * 2); o01 = (unsigned)p1 * (unsigned)(D * 2); o10 = (unsigned)p2 * (unsigned)(D * 2); o11 = (unsigned)p3 * (unsigned)(D * 2); return; }
;         const int* lp = list + u.e * T;
;         int v0 = lp[p0], v1 = lp[p1], v2 = lp[p2], v3 = lp[p3];
;         asm volatile("" : "+v"(v0), "+v"(v1), "+v"(v2), "+v"(v3));
;         const int c = cnt[u.e];
;         o00 = p0 < c ? (unsigned)v0 * (unsigned)(D * 2) : 0u; o01 = p1 < c ? (unsigned)v1 * (unsigned)(D * 2) : 0u;
;         o10 = p2 < c ? (unsigned)v2 * (unsigned)(D * 2) : 0u; o11 = p3 < c ? (unsigned)v3 * (unsigned)(D * 2) : 0u;
;     }
.LBB0_1814:
	s_or_b64 exec, exec, s[0:1]
	v_readlane_b32 s0, v254, 0
	v_readlane_b32 s1, v254, 1
	s_lshl_b32 s29, s28, 2
	v_readlane_b32 s2, v254, 5
	v_mov_b32_e32 v6, v0
	s_waitcnt lgkmcnt(0)
	s_barrier
	v_readlane_b32 s84, v254, 0
	v_readlane_b32 s85, v254, 1
	s_nop 1
	s_load_dwordx2 s[74:75], s[84:85], 0xe8
	s_load_dwordx2 s[78:79], s[84:85], 0x118
	v_and_b32_e32 v252, 63, v0
	v_lshrrev_b32_e32 v253, 6, v0
	v_lshlrev_b32_e32 v238, 2, v252
	v_lshlrev_b32_e32 v252, 4, v252
	v_add_u32_e32 v239, 0x2000, v238
	v_add_u32_e32 v240, 0x4000, v238
	v_add_u32_e32 v241, 0x6000, v238
	v_readlane_b32 s86, v254, 4
	v_readlane_b32 s87, v255, 40
	v_readfirstlane_b32 s88, v253
	s_nop 3
	s_lshl_b32 s71, s86, 3
	s_lshl_b32 s87, s87, 3
	s_add_u32 s87, s87, s88
	s_add_u32 s70, s87, 0x28000
	s_mov_b32 s80, 0
	s_mov_b32 s82, 0
	s_mov_b32 s90, 0
	s_waitcnt lgkmcnt(0)
	s_cmp_lt_i32 s2, s29
	s_nop 0
	v_readfirstlane_b32 s30, v6
	s_cbranch_scc0 .LBB0_1836
	v_ashrrev_i32_e32 v1, 31, v6
	v_lshrrev_b32_e32 v1, 26, v1
	v_add_u32_e32 v1, v6, v1
	v_ashrrev_i32_e32 v9, 6, v1
	v_bfe_i32 v1, v6, 27, 1
	v_lshlrev_b32_e32 v2, 4, v6
	v_lshrrev_b32_e32 v1, 22, v1
	v_add_u32_e32 v1, v2, v1
	v_and_b32_e32 v1, 0xfffffc00, v1
	v_sub_u32_e32 v1, v2, v1
	v_lshrrev_b32_e32 v3, 4, v1
	v_bitop3_b32 v10, v3, v1, 32 bitop3:0x6c
	v_ashrrev_i32_e32 v1, 31, v1
	v_lshrrev_b32_e32 v1, 26, v1
	s_load_dwordx2 s[0:1], s[0:1], 0x118
	v_lshlrev_b32_e32 v3, 3, v9
	v_add_u32_e32 v1, v10, v1
	v_and_b32_e32 v3, -16, v3
	v_ashrrev_i32_e32 v8, 6, v1
	v_add_u32_e32 v2, 0x2000, v2
	v_add_u32_e32 v1, v8, v3
	v_ashrrev_i32_e32 v3, 31, v2
	v_lshrrev_b32_e32 v3, 22, v3
	v_add_u32_e32 v3, v2, v3
	s_waitcnt lgkmcnt(0)
	s_add_u32 s31, s0, 0x3ec30000
	v_ashrrev_i32_e32 v11, 10, v3
	v_readlane_b32 s3, v254, 5
	s_addc_u32 s33, s1, 0
	v_mul_i32_i24_e32 v3, 0x400, v11
	s_and_b32 s2, s3, -4
	v_sub_u32_e32 v2, v2, v3
	s_add_i32 s2, s2, 0
	v_lshrrev_b32_e32 v3, 4, v2
	s_add_i32 s2, s2, 0x21160
	v_bitop3_b32 v12, v3, v2, 32 bitop3:0x6c
	v_mov_b32_e32 v3, s2
	ds_read_b32 v3, v3
	v_ashrrev_i32_e32 v4, 31, v12
	v_lshrrev_b32_e32 v4, 26, v4
	v_lshlrev_b32_e32 v2, 3, v11
	v_add_u32_e32 v4, v12, v4
	s_waitcnt lgkmcnt(0)
	v_lshlrev_b32_e32 v5, 2, v3
	v_add_u32_e32 v5, 0, v5
	v_add_u32_e32 v5, 0x21040, v5
	ds_read_b32 v5, v5
	v_and_b32_e32 v2, -16, v2
	v_ashrrev_i32_e32 v13, 6, v4
	s_ashr_i32 s8, s3, 2
	v_add_u32_e32 v146, v13, v2
	s_waitcnt lgkmcnt(0)
	v_sub_u32_e32 v2, s8, v5
	v_lshlrev_b32_e32 v7, 8, v2
	v_add_u32_e32 v2, v7, v1
	v_add_u32_e32 v4, v7, v146
	v_cmp_gt_i32_e32 vcc, 64, v3
	v_readfirstlane_b32 s6, v3
	v_add_u32_e32 v14, 0x80, v2
	v_add_u32_e32 v15, 0x80, v4
	s_cbranch_vccz .LBB0_1817
	s_lshl_b32 s2, s6, 13
	s_ashr_i32 s3, s2, 31
	s_lshl_b64 s[2:3], s[2:3], 2
	s_add_u32 s2, s31, s2
	s_addc_u32 s3, s33, s3
	v_ashrrev_i32_e32 v3, 31, v2
	v_lshl_add_u64 v[16:17], v[2:3], 2, s[2:3]
	v_ashrrev_i32_e32 v5, 31, v4
	v_lshl_add_u64 v[18:19], v[4:5], 2, s[2:3]
	global_load_dword v3, v[16:17], off
	global_load_dword v5, v[18:19], off
	global_load_dword v20, v[18:19], off offset:512
	global_load_dword v21, v[16:17], off offset:512
	s_lshl_b32 s2, s6, 2
	s_add_i32 s2, s2, 0
	s_add_i32 s2, s2, 0x21660
	v_mov_b32_e32 v16, s2
	s_waitcnt vmcnt(0)
	ds_read_b32 v17, v16
	v_lshlrev_b32_e32 v3, 12, v3
	v_lshlrev_b32_e32 v5, 12, v5
	v_lshlrev_b32_e32 v16, 12, v21
	v_lshlrev_b32_e32 v18, 12, v20
	s_waitcnt lgkmcnt(0)
	v_cmp_lt_i32_e32 vcc, v2, v17
	s_nop 1
	v_cndmask_b32_e32 v3, 0, v3, vcc
	v_cmp_lt_i32_e32 vcc, v4, v17
	s_nop 1
	v_cndmask_b32_e32 v5, 0, v5, vcc
	v_cmp_lt_i32_e32 vcc, v14, v17
	s_nop 1
	v_cndmask_b32_e32 v16, 0, v16, vcc
	v_cmp_lt_i32_e32 vcc, v15, v17
	s_nop 1
	v_cndmask_b32_e32 v17, 0, v18, vcc
	s_cbranch_execz .LBB0_1818
	s_branch .LBB0_1819

; __device__ __forceinline__ unsigned cvt_pk_bf16(float lo, float hi) { unsigned r; asm volatile("v_cvt_pk_bf16_f32 %0, %1, %2" : "=v"(r) : "v"(lo), "v"(hi)); return r; }
; #define PG8_STAGE(bufoff, gbase, v0, v1) do { \
;         __builtin_amdgcn_global_load_lds((const unsigned*)((const char*)(gbase) + (v0)), (LAS unsigned*)(lds + (bufoff) + ldsw), 16, 0, 0); \
;         __builtin_amdgcn_global_load_lds((const unsigned*)((const char*)(gbase) + (v1)), (LAS unsigned*)(lds + (bufoff) + ldsw + 8192), 16, 0, 0); } while (0)
; #define PG8_WAIT_V(n) asm volatile("s_waitcnt vmcnt(" #n ")" ::: "memory")
; template <class Epi, class Sched>
; __device__ __forceinline__ void gemm_phase(LAS unsigned char* lds, const int K, const Sched& S, const Epi& E) {
;     ...
;             PG8_LDB(B0, 0, 0); PG8_SCHED; PG8_LDA(At, 0, 0); PG8_STAGE(PG8_SA(1, 1), a1, c10, c11);
;             PG8_WAIT_L(8); PG8_BAR; PG8_WAIT_L(0); PG8_MMA(0, 0, At, B0); PG8_BAR; PG8_SCHED;
;             PG8_LDB(B1, 0, 1); PG8_STAGE(PG8_SB(0, 0), b2, voffB0, voffB1);
;             PG8_BAR; PG8_WAIT_L(0); PG8_MMA(0, 1, At, B1); PG8_BAR;
;             PG8_LDA(At, 0, 1); PG8_STAGE(PG8_SA(0, 0), a2, x00, x01);
;             PG8_BAR; PG8_WAIT_L(0); PG8_MMA(1, 0, At, B0); PG8_BAR; PG8_SCHED;
;             PG8_STAGE(PG8_SB(0, 1), b2 + hstep, voffB0, voffB1);
;             PG8_WAIT_V(6); PG8_BAR; PG8_MMA(1, 1, At, B1); PG8_BAR;
; template <int BANK, int WAITN> __device__ __forceinline__ void bg_finish1(BgState& b) {
;     if (WAITN == 32) asm volatile("s_waitcnt vmcnt(32)" ::: "memory"); else asm volatile("s_waitcnt vmcnt(0)" ::: "memory");
;     asm volatile("" : BG_TIE16(BANK * 32) :: "memory");
;     asm volatile("" : BG_TIE16(BANK * 32 + 16) :: "memory");
;     bf16_t* dst = b.dst[BANK];
;     if (dst != nullptr) {
; #pragma unroll
;         for (int c = 0; c < 4; ++c) { u32x4 w;
;             w.x = cvt_pk_bf16(b.r[(BANK * 8 + 0) * 4 + c], b.r[(BANK * 8 + 1) * 4 + c]); w.y = cvt_pk_bf16(b.r[(BANK * 8 + 2) * 4 + c], b.r[(BANK * 8 + 3) * 4 + c]);
;             w.z = cvt_pk_bf16(b.r[(BANK * 8 + 4) * 4 + c], b.r[(BANK * 8 + 5) * 4 + c]); w.w = cvt_pk_bf16(b.r[(BANK * 8 + 6) * 4 + c], b.r[(BANK * 8 + 7) * 4 + c]);
;             bf16_t* dp = dst + (c & 1) * 512 + (c >> 1) * b.o2[BANK];
;             asm volatile("global_store_dwordx4 %0, %1, off\n\ts_nop 1" :: "v"(dp), "v"(w) : "memory"); }
;     }
.LBB0_1831:
	v_add_u32_e32 v139, s46, v149
	s_add_u32 s22, s0, s20
	ds_read_b128 v[160:163], v139
	ds_read_b128 v[164:167], v139 offset:1024
	ds_read_b128 v[168:171], v139 offset:2048
	ds_read_b128 v[172:175], v139 offset:3072
	s_addc_u32 s23, s1, s21
	s_add_u32 s24, s22, 0x34c30100
	s_addc_u32 s25, s23, 0
	s_cmpk_eq_i32 s20, 0xf00
	s_cselect_b64 vcc, -1, 0
	s_and_b64 s[22:23], vcc, exec
	v_cndmask_b32_e32 v134, v158, v156, vcc
	s_cselect_b32 s27, s3, s25
	s_cselect_b32 s26, s2, s24
	v_cndmask_b32_e32 v139, v138, v154, vcc
	s_cselect_b32 s23, s19, s15
	s_cselect_b32 s22, s18, s13
	v_cndmask_b32_e32 v224, v136, v155, vcc
	s_add_u32 s24, s22, 0x20000
	s_addc_u32 s25, s23, 0
	v_lshl_add_u64 v[208:209], v[144:145], 0, s[20:21]
	s_add_i32 m0, s37, 0xc000
	ds_read_b128 v[176:179], v151
	ds_read_b128 v[180:183], v151 offset:1024
	ds_read_b128 v[184:187], v151 offset:2048
	ds_read_b128 v[188:191], v151 offset:3072
	ds_read_b128 v[192:195], v151 offset:4096
	ds_read_b128 v[196:199], v151 offset:5120
	ds_read_b128 v[200:203], v151 offset:6144
	ds_read_b128 v[204:207], v151 offset:7168
	global_load_lds_dwordx4 v[208:209], off
	v_lshl_add_u64 v[208:209], v[142:143], 0, s[20:21]
	s_add_i32 m0, s37, 0xe000
	s_nop 0
	global_load_lds_dwordx4 v[208:209], off
	s_waitcnt lgkmcnt(8)
	s_barrier
	s_waitcnt lgkmcnt(0)
	s_setprio 1
	s_waitcnt lgkmcnt(0)
	v_mfma_f32_16x16x32_bf16 v[126:129], v[160:163], v[176:179], v[126:129]
	v_mfma_f32_16x16x32_bf16 v[122:125], v[168:171], v[176:179], v[122:125]
	v_mfma_f32_16x16x32_bf16 v[110:113], v[160:163], v[184:187], v[110:113]
	v_mfma_f32_16x16x32_bf16 v[106:109], v[168:171], v[184:187], v[106:109]
	v_mfma_f32_16x16x32_bf16 v[94:97], v[160:163], v[192:195], v[94:97]
	v_mfma_f32_16x16x32_bf16 v[90:93], v[168:171], v[192:195], v[90:93]
	v_mfma_f32_16x16x32_bf16 v[78:81], v[160:163], v[200:203], v[78:81]
	v_mfma_f32_16x16x32_bf16 v[74:77], v[168:171], v[200:203], v[74:77]
	v_mfma_f32_16x16x32_bf16 v[126:129], v[164:167], v[180:183], v[126:129]
	v_mfma_f32_16x16x32_bf16 v[122:125], v[172:175], v[180:183], v[122:125]
	v_mfma_f32_16x16x32_bf16 v[110:113], v[164:167], v[188:191], v[110:113]
	v_mfma_f32_16x16x32_bf16 v[106:109], v[172:175], v[188:191], v[106:109]
	v_mfma_f32_16x16x32_bf16 v[94:97], v[164:167], v[196:199], v[94:97]
	v_mfma_f32_16x16x32_bf16 v[90:93], v[172:175], v[196:199], v[90:93]
	v_mfma_f32_16x16x32_bf16 v[78:81], v[164:167], v[204:207], v[78:81]
	v_mfma_f32_16x16x32_bf16 v[74:77], v[172:175], v[204:207], v[74:77]
	s_setprio 0
	s_barrier
	s_add_i32 s54, s46, s36
	v_add_u32_e32 v141, s48, v149
	v_lshl_add_u64 v[226:227], s[22:23], 0, v[130:131]
	s_mov_b32 m0, s54
	ds_read_b128 v[208:211], v141
	ds_read_b128 v[212:215], v141 offset:1024
	ds_read_b128 v[216:219], v141 offset:2048
	ds_read_b128 v[220:223], v141 offset:3072
	global_load_lds_dwordx4 v[226:227], off
	v_lshl_add_u64 v[228:229], s[22:23], 0, v[132:133]
	s_add_i32 m0, s54, 0x2000
	s_nop 0
	global_load_lds_dwordx4 v[228:229], off
	s_barrier
	s_waitcnt lgkmcnt(0)
	s_setprio 1
	s_waitcnt lgkmcnt(0)
	v_mfma_f32_16x16x32_bf16 v[118:121], v[208:211], v[176:179], v[118:121]
	v_mfma_f32_16x16x32_bf16 v[114:117], v[216:219], v[176:179], v[114:117]
	v_mfma_f32_16x16x32_bf16 v[102:105], v[208:211], v[184:187], v[102:105]
	v_mfma_f32_16x16x32_bf16 v[98:101], v[216:219], v[184:187], v[98:101]
	v_mfma_f32_16x16x32_bf16 v[86:89], v[208:211], v[192:195], v[86:89]
	v_mfma_f32_16x16x32_bf16 v[82:85], v[216:219], v[192:195], v[82:85]
	v_mfma_f32_16x16x32_bf16 v[70:73], v[208:211], v[200:203], v[70:73]
	v_mfma_f32_16x16x32_bf16 v[66:69], v[216:219], v[200:203], v[66:69]
	v_mfma_f32_16x16x32_bf16 v[118:121], v[212:215], v[180:183], v[118:121]
	v_mfma_f32_16x16x32_bf16 v[114:117], v[220:223], v[180:183], v[114:117]
	v_mfma_f32_16x16x32_bf16 v[102:105], v[212:215], v[188:191], v[102:105]
	v_mfma_f32_16x16x32_bf16 v[98:101], v[220:223], v[188:191], v[98:101]
	v_mfma_f32_16x16x32_bf16 v[86:89], v[212:215], v[196:199], v[86:89]
	v_mfma_f32_16x16x32_bf16 v[82:85], v[220:223], v[196:199], v[82:85]
	v_mfma_f32_16x16x32_bf16 v[70:73], v[212:215], v[204:207], v[70:73]
	v_mfma_f32_16x16x32_bf16 v[66:69], v[220:223], v[204:207], v[66:69]
	s_setprio 0
	s_mov_b32 m0, s37
	s_barrier
	ds_read_b128 v[176:179], v151 offset:16384
	ds_read_b128 v[180:183], v151 offset:17408
	ds_read_b128 v[184:187], v151 offset:18432
	ds_read_b128 v[188:191], v151 offset:19456
	ds_read_b128 v[192:195], v151 offset:20480
	ds_read_b128 v[196:199], v151 offset:21504
	ds_read_b128 v[200:203], v151 offset:22528
	ds_read_b128 v[204:207], v151 offset:23552
	global_load_lds_dwordx4 v134, s[26:27]
	s_mov_b32 m0, s38
	v_mov_b32_e32 v225, v135
	global_load_lds_dwordx4 v224, s[26:27]
	s_barrier
	s_waitcnt lgkmcnt(0)
	v_lshl_add_u64 v[230:231], s[26:27], 0, v[134:135]
	v_lshl_add_u64 v[224:225], s[26:27], 0, v[224:225]
	s_setprio 1
	s_waitcnt lgkmcnt(0)
	v_mfma_f32_16x16x32_bf16 v[62:65], v[160:163], v[176:179], v[62:65]
	v_mfma_f32_16x16x32_bf16 v[58:61], v[168:171], v[176:179], v[58:61]
	v_mfma_f32_16x16x32_bf16 v[46:49], v[160:163], v[184:187], v[46:49]
	v_mfma_f32_16x16x32_bf16 v[42:45], v[168:171], v[184:187], v[42:45]
	v_mfma_f32_16x16x32_bf16 v[30:33], v[160:163], v[192:195], v[30:33]
	v_mfma_f32_16x16x32_bf16 v[26:29], v[168:171], v[192:195], v[26:29]
	v_mfma_f32_16x16x32_bf16 v[14:17], v[160:163], v[200:203], v[14:17]
	v_mfma_f32_16x16x32_bf16 v[10:13], v[168:171], v[200:203], v[10:13]
	v_mfma_f32_16x16x32_bf16 v[62:65], v[164:167], v[180:183], v[62:65]
	v_mfma_f32_16x16x32_bf16 v[58:61], v[172:175], v[180:183], v[58:61]
	v_mfma_f32_16x16x32_bf16 v[46:49], v[164:167], v[188:191], v[46:49]
	v_mfma_f32_16x16x32_bf16 v[42:45], v[172:175], v[188:191], v[42:45]
	v_mfma_f32_16x16x32_bf16 v[30:33], v[164:167], v[196:199], v[30:33]
	v_mfma_f32_16x16x32_bf16 v[26:29], v[172:175], v[196:199], v[26:29]
	v_mfma_f32_16x16x32_bf16 v[14:17], v[164:167], v[204:207], v[14:17]
	v_mfma_f32_16x16x32_bf16 v[10:13], v[172:175], v[204:207], v[10:13]
	s_setprio 0
	s_barrier
	s_add_i32 s54, s48, s36
	v_lshl_add_u64 v[160:161], v[226:227], 0, s[4:5]
	s_mov_b32 m0, s54
	s_nop 0
	global_load_lds_dwordx4 v[160:161], off
	v_lshl_add_u64 v[160:161], v[228:229], 0, s[4:5]
	s_add_i32 m0, s54, 0x2000
	s_nop 0
	global_load_lds_dwordx4 v[160:161], off
	s_cmp_eq_u32 s82, 0
	s_cbranch_scc1 .Lpb17_p4n
	s_waitcnt vmcnt(8)
	v_cvt_pk_bf16_f32 v244, v244, v245
	v_cvt_pk_bf16_f32 v245, v246, v247
	v_cvt_pk_bf16_f32 v246, v248, v249
	v_cvt_pk_bf16_f32 v247, v250, v251
	global_store_dwordx4 v253, v[244:247], s[78:79]
	s_mov_b32 s82, 0
	s_waitcnt vmcnt(7)
	s_branch .Lpb17_p4j

; #define PG8_STAGE(bufoff, gbase, v0, v1) do { \
;         __builtin_amdgcn_global_load_lds((const unsigned*)((const char*)(gbase) + (v0)), (LAS unsigned*)(lds + (bufoff) + ldsw), 16, 0, 0); \
;         __builtin_amdgcn_global_load_lds((const unsigned*)((const char*)(gbase) + (v1)), (LAS unsigned*)(lds + (bufoff) + ldsw + 8192), 16, 0, 0); } while (0)
; #define PG8_LDA(dst, b, h) do { _Pragma("unroll") for (int m = 0; m < 4; ++m) _Pragma("unroll") for (int k = 0; k < 2; ++k) dst[m][k] = *(const LAS bf16x8*)(lds + PG8_SA(b, h) + aoff + m * 2048 + k * 1024); } while (0)
; #define PG8_LDB(dst, b, h) do { _Pragma("unroll") for (int n = 0; n < 2; ++n) _Pragma("unroll") for (int k = 0; k < 2; ++k) dst[n][k] = *(const LAS bf16x8*)(lds + PG8_SB(b, h) + boff + n * 2048 + k * 1024); } while (0)
; #define PG8_MMA(ai, bj, At, Bt) do { __builtin_amdgcn_s_setprio(1); _Pragma("unroll") for (int m = 0; m < 4; ++m) _Pragma("unroll") for (int n = 0; n < 2; ++n) _Pragma("unroll") for (int k = 0; k < 2; ++k) \
;         acc[ai][bj][m][n] = __builtin_amdgcn_mfma_f32_16x16x32_bf16(Bt[n][k], At[m][k], acc[ai][bj][m][n], 0, 0, 0); __builtin_amdgcn_s_setprio(0); } while (0)
; #define PG8_WAIT_V(n) asm volatile("s_waitcnt vmcnt(" #n ")" ::: "memory")
; #define PG8_WAIT_L(n) asm volatile("s_waitcnt lgkmcnt(" #n ")" ::: "memory")
; #define PG8_BAR __builtin_amdgcn_s_barrier()
; #define PG8_SCHED __builtin_amdgcn_sched_barrier(0)
; template <class Epi, class Sched>
; __device__ __forceinline__ void gemm_phase(LAS unsigned char* lds, const int K, const Sched& S, const Epi& E) {
;     ...
;             PG8_WAIT_V(6); PG8_BAR; PG8_MMA(1, 1, At, B1); PG8_BAR;
;             PG8_LDB(B0, 1, 0); PG8_SCHED; PG8_LDA(At, 1, 0); PG8_STAGE(PG8_SA(0, 1), a2, x10, x11);
;             PG8_WAIT_L(8); PG8_BAR; PG8_WAIT_L(0); PG8_MMA(0, 0, At, B0); PG8_BAR; PG8_SCHED;
;             PG8_LDB(B1, 1, 1); PG8_STAGE(PG8_SB(1, 0), b3, voffB0, voffB1);
;             PG8_BAR; PG8_WAIT_L(0); PG8_MMA(0, 1, At, B1); PG8_BAR;
.Lpb17_p4j:
	s_barrier
	s_setprio 1
	v_mfma_f32_16x16x32_bf16 v[54:57], v[208:211], v[176:179], v[54:57]
	v_mfma_f32_16x16x32_bf16 v[50:53], v[216:219], v[176:179], v[50:53]
	v_mfma_f32_16x16x32_bf16 v[38:41], v[208:211], v[184:187], v[38:41]
	v_mfma_f32_16x16x32_bf16 v[34:37], v[216:219], v[184:187], v[34:37]
	v_mfma_f32_16x16x32_bf16 v[22:25], v[208:211], v[192:195], v[22:25]
	v_mfma_f32_16x16x32_bf16 v[18:21], v[216:219], v[192:195], v[18:21]
	v_mfma_f32_16x16x32_bf16 v[6:9], v[208:211], v[200:203], v[6:9]
	v_mfma_f32_16x16x32_bf16 v[2:5], v[216:219], v[200:203], v[2:5]
	v_mfma_f32_16x16x32_bf16 v[54:57], v[212:215], v[180:183], v[54:57]
	v_mfma_f32_16x16x32_bf16 v[50:53], v[220:223], v[180:183], v[50:53]
	v_mfma_f32_16x16x32_bf16 v[38:41], v[212:215], v[188:191], v[38:41]
	v_mfma_f32_16x16x32_bf16 v[34:37], v[220:223], v[188:191], v[34:37]
	v_mfma_f32_16x16x32_bf16 v[22:25], v[212:215], v[196:199], v[22:25]
	v_mfma_f32_16x16x32_bf16 v[18:21], v[220:223], v[196:199], v[18:21]
	v_mfma_f32_16x16x32_bf16 v[6:9], v[212:215], v[204:207], v[6:9]
	v_mfma_f32_16x16x32_bf16 v[2:5], v[220:223], v[204:207], v[2:5]
	s_setprio 0
	s_add_i32 s54, 0, 0x18000
	v_add_u32_e32 v134, s54, v149
	s_barrier
	ds_read_b128 v[160:163], v134
	ds_read_b128 v[164:167], v134 offset:1024
	ds_read_b128 v[168:171], v134 offset:2048
	ds_read_b128 v[172:175], v134 offset:3072
	s_mov_b32 m0, s39
	ds_read_b128 v[176:179], v151 offset:32768
	ds_read_b128 v[180:183], v151 offset:33792
	ds_read_b128 v[184:187], v151 offset:34816
	ds_read_b128 v[188:191], v151 offset:35840
	ds_read_b128 v[192:195], v151 offset:36864
	ds_read_b128 v[196:199], v151 offset:37888
	ds_read_b128 v[200:203], v151 offset:38912
	ds_read_b128 v[204:207], v151 offset:39936
	v_cndmask_b32_e32 v134, v140, v153, vcc
	global_load_lds_dwordx4 v139, s[26:27]
	s_mov_b32 m0, s40
	s_nop 0
	global_load_lds_dwordx4 v134, s[26:27]
	s_waitcnt lgkmcnt(8)
	s_barrier
	s_waitcnt lgkmcnt(0)
	s_setprio 1
	s_waitcnt lgkmcnt(0)
	v_mfma_f32_16x16x32_bf16 v[126:129], v[160:163], v[176:179], v[126:129]
	v_mfma_f32_16x16x32_bf16 v[122:125], v[168:171], v[176:179], v[122:125]
	v_mfma_f32_16x16x32_bf16 v[110:113], v[160:163], v[184:187], v[110:113]
	v_mfma_f32_16x16x32_bf16 v[106:109], v[168:171], v[184:187], v[106:109]
	v_mfma_f32_16x16x32_bf16 v[94:97], v[160:163], v[192:195], v[94:97]
	v_mfma_f32_16x16x32_bf16 v[90:93], v[168:171], v[192:195], v[90:93]
	v_mfma_f32_16x16x32_bf16 v[78:81], v[160:163], v[200:203], v[78:81]
	v_mfma_f32_16x16x32_bf16 v[74:77], v[168:171], v[200:203], v[74:77]
	v_mfma_f32_16x16x32_bf16 v[126:129], v[164:167], v[180:183], v[126:129]
	v_mfma_f32_16x16x32_bf16 v[122:125], v[172:175], v[180:183], v[122:125]
	v_mfma_f32_16x16x32_bf16 v[110:113], v[164:167], v[188:191], v[110:113]
	v_mfma_f32_16x16x32_bf16 v[106:109], v[172:175], v[188:191], v[106:109]
	v_mfma_f32_16x16x32_bf16 v[94:97], v[164:167], v[196:199], v[94:97]
	v_mfma_f32_16x16x32_bf16 v[90:93], v[172:175], v[196:199], v[90:93]
	v_mfma_f32_16x16x32_bf16 v[78:81], v[164:167], v[204:207], v[78:81]
	v_mfma_f32_16x16x32_bf16 v[74:77], v[172:175], v[204:207], v[74:77]
	s_setprio 0
	s_barrier
	s_add_i32 s26, 0, 0x1c000
	s_add_i32 s27, s54, s36
	v_add_u32_e32 v134, s26, v149
	v_lshl_add_u64 v[226:227], s[24:25], 0, v[130:131]
	s_mov_b32 m0, s27
	ds_read_b128 v[208:211], v134
	ds_read_b128 v[212:215], v134 offset:1024
	ds_read_b128 v[216:219], v134 offset:2048
	ds_read_b128 v[220:223], v134 offset:3072
	global_load_lds_dwordx4 v[226:227], off
	v_lshl_add_u64 v[226:227], s[24:25], 0, v[132:133]
	s_add_i32 m0, s27, 0x2000
	s_nop 0
	global_load_lds_dwordx4 v[226:227], off
	s_barrier
; #define PG8_STAGE(bufoff, gbase, v0, v1) do { \
;         __builtin_amdgcn_global_load_lds((const unsigned*)((const char*)(gbase) + (v0)), (LAS unsigned*)(lds + (bufoff) + ldsw), 16, 0, 0); \
;         __builtin_amdgcn_global_load_lds((const unsigned*)((const char*)(gbase) + (v1)), (LAS unsigned*)(lds + (bufoff) + ldsw + 8192), 16, 0, 0); } while (0)
; #define PG8_LDA(dst, b, h) do { _Pragma("unroll") for (int m = 0; m < 4; ++m) _Pragma("unroll") for (int k = 0; k < 2; ++k) dst[m][k] = *(const LAS bf16x8*)(lds + PG8_SA(b, h) + aoff + m * 2048 + k * 1024); } while (0)
; #define PG8_WAIT_V(n) asm volatile("s_waitcnt vmcnt(" #n ")" ::: "memory")
; #define PG8_WAIT_L(n) asm volatile("s_waitcnt lgkmcnt(" #n ")" ::: "memory")
; template <class Epi, class Sched>
; __device__ __forceinline__ void gemm_phase(LAS unsigned char* lds, const int K, const Sched& S, const Epi& E) {
;     ...
;             PG8_BAR; PG8_WAIT_L(0); PG8_MMA(0, 1, At, B1); PG8_BAR;
;             PG8_LDA(At, 1, 1); PG8_STAGE(PG8_SA(1, 0), a3, x00, x01);
;             PG8_BAR; PG8_WAIT_L(0); PG8_MMA(1, 0, At, B0); PG8_BAR; PG8_SCHED;
;             PG8_STAGE(PG8_SB(1, 1), b3 + hstep, voffB0, voffB1);
;             PG8_WAIT_V(6); PG8_BAR; PG8_MMA(1, 1, At, B1); PG8_BAR;
; __device__ __forceinline__ bool bg_decode(int st, int wg, int NW, int lane, KP kp, const float*& src, int& ldS, bf16_t*& dst, int& o2) {
;     const int g = st * NW + wg;
;     if (g >= BG_STEPS) { src = kp->in[27] + lane; ldS = 0; dst = nullptr; o2 = 0; return false; }
;     const int l = g / 98304, r = g - l * 98304;
;     unsigned char* ws = kp->ws;
;     if (r < 65536) {
;         const int e = r >> 10, kc = (r >> 2) & 255, kind = (r >> 1) & 1, cc = r & 1, n = cc * 256 + lane;
;         ldS = FF; o2 = 256 * 8;
;         src = kp->in[27 + kind] + ((size_t)(l * NE + e) * D + kc * 8) * FF + n;
;         const int drow = (n >> 7) * 256 + kind * 128 + (n & 127);
;         dst = (bf16_t*)(ws + WS_WGU) + l * WGU_L + (size_t)e * 1024 * D + ((size_t)kc * 1024 + drow) * 8;
;     } else {
;         const int r2 = r - 65536, e = r2 >> 9, kc = (r2 >> 3) & 63, cc = r2 & 7, n = cc * 256 + lane;
;         ldS = D; o2 = 128 * 8;
;         src = kp->in[29] + ((size_t)(l * NE + e) * FF + kc * 8) * D + n;
;         dst = (bf16_t*)(ws + WS_WD) + l * WD_L + (size_t)e * D * FF + ((size_t)kc * D + n) * 8;
;     }
;     return true;
; }
	s_waitcnt lgkmcnt(0)
	s_setprio 1
	s_waitcnt lgkmcnt(0)
	v_mfma_f32_16x16x32_bf16 v[118:121], v[208:211], v[176:179], v[118:121]
	v_mfma_f32_16x16x32_bf16 v[114:117], v[216:219], v[176:179], v[114:117]
	v_mfma_f32_16x16x32_bf16 v[102:105], v[208:211], v[184:187], v[102:105]
	v_mfma_f32_16x16x32_bf16 v[98:101], v[216:219], v[184:187], v[98:101]
	v_mfma_f32_16x16x32_bf16 v[86:89], v[208:211], v[192:195], v[86:89]
	v_mfma_f32_16x16x32_bf16 v[82:85], v[216:219], v[192:195], v[82:85]
	v_mfma_f32_16x16x32_bf16 v[70:73], v[208:211], v[200:203], v[70:73]
	v_mfma_f32_16x16x32_bf16 v[66:69], v[216:219], v[200:203], v[66:69]
	v_mfma_f32_16x16x32_bf16 v[118:121], v[212:215], v[180:183], v[118:121]
	v_mfma_f32_16x16x32_bf16 v[114:117], v[220:223], v[180:183], v[114:117]
	v_mfma_f32_16x16x32_bf16 v[102:105], v[212:215], v[188:191], v[102:105]
	v_mfma_f32_16x16x32_bf16 v[98:101], v[220:223], v[188:191], v[98:101]
	v_mfma_f32_16x16x32_bf16 v[86:89], v[212:215], v[196:199], v[86:89]
	v_mfma_f32_16x16x32_bf16 v[82:85], v[220:223], v[196:199], v[82:85]
	v_mfma_f32_16x16x32_bf16 v[70:73], v[212:215], v[204:207], v[70:73]
	v_mfma_f32_16x16x32_bf16 v[66:69], v[220:223], v[204:207], v[66:69]
	s_setprio 0
	s_mov_b32 m0, s43
	v_lshl_add_u64 v[226:227], v[230:231], 0, s[10:11]
	s_barrier
	ds_read_b128 v[176:179], v151 offset:49152
	ds_read_b128 v[180:183], v151 offset:50176
	ds_read_b128 v[184:187], v151 offset:51200
	ds_read_b128 v[188:191], v151 offset:52224
	ds_read_b128 v[192:195], v151 offset:53248
	ds_read_b128 v[196:199], v151 offset:54272
	ds_read_b128 v[200:203], v151 offset:55296
	ds_read_b128 v[204:207], v151 offset:56320
	global_load_lds_dwordx4 v[226:227], off
	v_lshl_add_u64 v[224:225], v[224:225], 0, s[10:11]
	s_mov_b32 m0, s44
	s_nop 0
	global_load_lds_dwordx4 v[224:225], off
	s_barrier
	s_waitcnt lgkmcnt(0)
	s_setprio 1
	s_waitcnt lgkmcnt(0)
	v_mfma_f32_16x16x32_bf16 v[62:65], v[160:163], v[176:179], v[62:65]
	v_mfma_f32_16x16x32_bf16 v[58:61], v[168:171], v[176:179], v[58:61]
	v_mfma_f32_16x16x32_bf16 v[46:49], v[160:163], v[184:187], v[46:49]
	v_mfma_f32_16x16x32_bf16 v[42:45], v[168:171], v[184:187], v[42:45]
	v_mfma_f32_16x16x32_bf16 v[30:33], v[160:163], v[192:195], v[30:33]
	v_mfma_f32_16x16x32_bf16 v[26:29], v[168:171], v[192:195], v[26:29]
	v_mfma_f32_16x16x32_bf16 v[14:17], v[160:163], v[200:203], v[14:17]
	v_mfma_f32_16x16x32_bf16 v[10:13], v[168:171], v[200:203], v[10:13]
	v_mfma_f32_16x16x32_bf16 v[62:65], v[164:167], v[180:183], v[62:65]
	v_mfma_f32_16x16x32_bf16 v[58:61], v[172:175], v[180:183], v[58:61]
	v_mfma_f32_16x16x32_bf16 v[46:49], v[164:167], v[188:191], v[46:49]
	v_mfma_f32_16x16x32_bf16 v[42:45], v[172:175], v[188:191], v[42:45]
	v_mfma_f32_16x16x32_bf16 v[30:33], v[164:167], v[196:199], v[30:33]
	v_mfma_f32_16x16x32_bf16 v[26:29], v[172:175], v[196:199], v[26:29]
	v_mfma_f32_16x16x32_bf16 v[14:17], v[164:167], v[204:207], v[14:17]
	v_mfma_f32_16x16x32_bf16 v[10:13], v[172:175], v[204:207], v[10:13]
	s_setprio 0
	s_barrier
	s_add_u32 s22, s22, 0x20800
	s_addc_u32 s23, s23, 0
	s_add_i32 s24, s26, s36
	v_lshl_add_u64 v[160:161], s[22:23], 0, v[130:131]
	s_mov_b32 m0, s24
	s_nop 0
	global_load_lds_dwordx4 v[160:161], off
	v_lshl_add_u64 v[160:161], s[22:23], 0, v[132:133]
	s_add_i32 m0, s24, 0x2000
	s_nop 0
	global_load_lds_dwordx4 v[160:161], off
	s_cmp_ge_u32 s70, 0x30000
	s_cbranch_scc1 .Lpb17_p8n
	s_cmp_eq_u32 s80, 0
	s_cbranch_scc0 .Lpb17_adv4
	s_cmp_ge_u32 s70, 0x28000
	s_mov_b32 s84, 0x10000
	s_cselect_b32 s84, 0x28000, s84
	s_cselect_b32 s83, 0x10000000, 0
	s_mov_b32 s81, 0x24830000
	s_cselect_b32 s81, 0x2ca30000, s81
	s_sub_u32 s84, s70, s84
	s_lshr_b32 s85, s84, 3
	s_and_b32 s86, s84, 7
	s_lshl_b32 s87, s85, 16
	s_lshl_b32 s84, s86, 10
	s_add_u32 s87, s87, s84
	s_add_u32 s87, s87, s83
	s_add_u32 s72, s74, s87
	s_addc_u32 s73, s75, 0
	s_add_u32 s88, s72, 0x8000
	s_addc_u32 s89, s73, 0
	s_lshl_b32 s85, s85, 15
	s_lshl_b32 s86, s86, 12
	s_add_u32 s85, s85, s86
	s_add_u32 s85, s85, s81
	v_add_u32_e32 v253, s85, v252
	s_branch .Lpb17_ld4
.Lpb17_adv4:
	v_add_u32_e32 v253, 0x400, v253
	s_add_u32 s72, s72, 0x100
	s_addc_u32 s73, s73, 0
	s_add_u32 s88, s88, 0x100
	s_addc_u32 s89, s89, 0

; __device__ __forceinline__ bool bg_decode(int st, int wg, int NW, int lane, KP kp, const float*& src, int& ldS, bf16_t*& dst, int& o2) {
;     const int g = st * NW + wg;
;     if (g >= BG_STEPS) { src = kp->in[27] + lane; ldS = 0; dst = nullptr; o2 = 0; return false; }
;     const int l = g / 98304, r = g - l * 98304;
;     unsigned char* ws = kp->ws;
;     if (r < 65536) {
;         const int e = r >> 10, kc = (r >> 2) & 255, kind = (r >> 1) & 1, cc = r & 1, n = cc * 256 + lane;
;         ldS = FF; o2 = 256 * 8;
;         src = kp->in[27 + kind] + ((size_t)(l * NE + e) * D + kc * 8) * FF + n;
;         const int drow = (n >> 7) * 256 + kind * 128 + (n & 127);
;         dst = (bf16_t*)(ws + WS_WGU) + l * WGU_L + (size_t)e * 1024 * D + ((size_t)kc * 1024 + drow) * 8;
;     } else {
;         const int r2 = r - 65536, e = r2 >> 9, kc = (r2 >> 3) & 63, cc = r2 & 7, n = cc * 256 + lane;
;         ldS = D; o2 = 128 * 8;
;         src = kp->in[29] + ((size_t)(l * NE + e) * FF + kc * 8) * D + n;
;         dst = (bf16_t*)(ws + WS_WD) + l * WD_L + (size_t)e * D * FF + ((size_t)kc * D + n) * 8;
;     }
;     return true;
; }
.Lpb17_d1:
	s_cmp_ge_u32 s70, 0x30000
	s_cbranch_scc1 .Lpb17_dend
	s_cmp_eq_u32 s80, 0
	s_cbranch_scc0 .Lpb17_adv3
	s_cmp_ge_u32 s70, 0x28000
	s_mov_b32 s84, 0x10000
	s_cselect_b32 s84, 0x28000, s84
	s_cselect_b32 s83, 0x10000000, 0
	s_mov_b32 s81, 0x24830000
	s_cselect_b32 s81, 0x2ca30000, s81
	s_sub_u32 s84, s70, s84
	s_lshr_b32 s85, s84, 3
	s_and_b32 s86, s84, 7
	s_lshl_b32 s87, s85, 16
	s_lshl_b32 s84, s86, 10
	s_add_u32 s87, s87, s84
	s_add_u32 s87, s87, s83
	s_add_u32 s72, s74, s87
	s_addc_u32 s73, s75, 0
	s_add_u32 s88, s72, 0x8000
	s_addc_u32 s89, s73, 0
	s_lshl_b32 s85, s85, 15
	s_lshl_b32 s86, s86, 12
	s_add_u32 s85, s85, s86
	s_add_u32 s85, s85, s81
	v_add_u32_e32 v253, s85, v252
	s_branch .Lpb17_ld3
